# v48 + relay atomic removed: an XCD's last arriver is also released by the top-level generation word (one atomic ack round trip less per grid barrier)
# speedup vs baseline: 1.0094x; 1.0040x over previous
.LBB0_17:
	s_or_b64 exec, exec, s[0:1]
	s_add_i32 s92, s18, 0x900
	s_lshl_b64 s[0:1], s[92:93], 2
	v_lshl_add_u64 v[4:5], v[4:5], 0, s[0:1]
	v_mov_b32_e32 v1, 1
	s_waitcnt vmcnt(0) lgkmcnt(0)
	buffer_inv sc1
	s_waitcnt vmcnt(0)

.LBB0_1123:
	s_or_b64 exec, exec, s[0:1]
	s_add_i32 s92, s20, 0x900
	s_lshl_b64 s[0:1], s[92:93], 2
	v_lshl_add_u64 v[4:5], v[4:5], 0, s[0:1]
	v_mov_b32_e32 v1, 1
	s_waitcnt vmcnt(0) lgkmcnt(0)
	buffer_inv sc1
	s_waitcnt vmcnt(0)
